# speedup vs baseline: 1.0524x; 1.0524x over previous
_Z8pam_mainPKDv4_jS1_S1_PKfS3_PDF16_Pf:
	s_load_dwordx8 s[4:11], s[0:1], 0x0
	s_load_dwordx4 s[12:15], s[0:1], 0x20
	s_load_dwordx2 s[16:17], s[0:1], 0x30
	v_and_b32_e32 v1, 63, v0
	v_lshrrev_b32_e32 v3, 6, v0
	v_lshlrev_b32_e32 v2, 4, v1
	v_lshlrev_b32_e32 v4, 2, v1
	v_readfirstlane_b32 s18, v3
	v_and_b32_e32 v3, 31, v1
	v_lshlrev_b32_e32 v5, 2, v3
	s_mul_i32 s19, s2, 54
	s_mul_i32 s20, s2, 3
	s_lshr_b32 s20, s20, 4
	s_mul_i32 s21, s20, 0x120
	s_sub_u32 s21, s19, s21
	s_cmp_ge_u32 s20, 24
	s_cselect_b32 s22, 0x120, 0
	s_add_u32 s22, s22, s21
	s_add_u32 s23, s20, 1
	s_cmp_ge_u32 s23, 24
	s_cselect_b32 s24, 0x120, 0
	s_sub_u32 s25, 0x120, s21
	s_cmp_lt_u32 s25, 54
	s_cselect_b32 s26, 1, 0
	s_mul_i32 s25, s25, 43
	s_lshr_b32 s25, s25, 8
	s_cmp_eq_u32 s26, 1
	s_cselect_b32 s25, s25, 100
	s_mov_b32 s29, s2
	s_mov_b32 s46, 0
	s_mov_b32 s47, 30720
	s_mov_b32 s48, 61440
	s_mov_b32 s27, 0
	s_mov_b32 s28, 1
	s_mul_i32 s30, s18, 0xd00
	s_add_u32 s30, s30, 92160
	v_add_u32_e32 v7, s30, v2
	v_mul_u32_u24_e32 v6, 0x68, v3
	v_lshrrev_b32_e32 v130, 2, v1
	v_and_b32_e32 v130, 8, v130
	v_add3_u32 v6, v6, v130, s30
	v_mov_b32_e32 v150, 0xf149f2ca
	s_waitcnt lgkmcnt(0)
	s_sub_u32 s30, s27, s25
	s_mul_i32 s30, s30, 6
	s_add_u32 s30, s30, s24
	s_mul_i32 s31, s27, 6
	s_add_u32 s31, s31, s22
	s_cmp_lt_u32 s27, s25
	s_cselect_b32 s30, s31, s30
	s_lshl_b32 s33, s18, 10
	s_lshl_b32 s31, s30, 12
	s_add_u32 s31, s31, s33
	s_add_u32 s50, s8, s31
	s_addc_u32 s51, s9, 0
	s_add_u32 s52, s50, 0x3000
	s_addc_u32 s53, s51, 0
	s_add_u32 s34, s46, s33
	s_mov_b32 m0, s34
	s_add_u32 s35, s34, 0x3000
	global_load_lds_dwordx4 v2, s[50:51]
	s_mov_b32 m0, s35
	s_nop 0
	global_load_lds_dwordx4 v2, s[52:53]
	s_cmp_lt_u32 s18, 6
	s_cbranch_scc0 .Lm_nok_p0
	s_lshl_b32 s31, s30, 10
	s_add_u32 s31, s31, s33
	s_add_u32 s54, s4, s31
	s_addc_u32 s55, s5, 0
	s_add_u32 s34, s34, 24576
	s_mov_b32 m0, s34
	s_nop 0
	global_load_lds_dwordx4 v2, s[54:55]
.Lm_nok_p0:
	global_load_dwordx4 v[132:135], v2, s[12:13]
	global_load_dwordx4 v[136:139], v2, s[12:13] offset:1024
	global_load_dword v140, v4, s[12:13] offset:2048
	s_mul_i32 s30, s20, 12
	s_add_u32 s30, s30, s18
	s_add_u32 s31, s20, s26
	s_mul_i32 s31, s31, 12
	s_add_u32 s31, s31, s18
	s_lshl_b32 s36, s30, 10
	s_add_u32 s56, s6, s36
	s_addc_u32 s57, s7, 0
	s_lshl_b32 s36, s31, 10
	s_add_u32 s58, s6, s36
	s_addc_u32 s59, s7, 0
	global_load_dwordx4 v[8:11], v2, s[56:57]
	global_load_dwordx4 v[12:15], v2, s[58:59]
	s_lshl_b32 s36, s30, 7
	s_add_u32 s60, s10, s36
	s_addc_u32 s61, s11, 0
	s_lshl_b32 s36, s31, 7
	s_add_u32 s62, s10, s36
	s_addc_u32 s63, s11, 0
	global_load_dword v141, v5, s[60:61]
	global_load_dword v142, v5, s[62:63]
	s_sub_u32 s30, s28, s25
	s_mul_i32 s30, s30, 6
	s_add_u32 s30, s30, s24
	s_mul_i32 s31, s28, 6
	s_add_u32 s31, s31, s22
	s_cmp_lt_u32 s28, s25
	s_cselect_b32 s30, s31, s30
	s_lshl_b32 s33, s18, 10
	s_lshl_b32 s31, s30, 12
	s_add_u32 s31, s31, s33
	s_add_u32 s50, s8, s31
	s_addc_u32 s51, s9, 0
	s_add_u32 s52, s50, 0x3000
	s_addc_u32 s53, s51, 0
	s_add_u32 s34, s47, s33
	s_mov_b32 m0, s34
	s_add_u32 s35, s34, 0x3000
	global_load_lds_dwordx4 v2, s[50:51]
	s_mov_b32 m0, s35
	s_nop 0
	global_load_lds_dwordx4 v2, s[52:53]
	s_cmp_lt_u32 s18, 6
	s_cbranch_scc0 .Lm_nok_p1
	s_lshl_b32 s31, s30, 10
	s_add_u32 s31, s31, s33
	s_add_u32 s54, s4, s31
	s_addc_u32 s55, s5, 0
	s_add_u32 s34, s34, 24576
	s_mov_b32 m0, s34
	s_nop 0
	global_load_lds_dwordx4 v2, s[54:55]
.Lm_nok_p1:
	s_waitcnt vmcnt(2)
	s_nop 0
	v_max3_f32 v132, v132, v133, v134
	v_max3_f32 v136, v136, v137, v138
	v_max3_f32 v132, v132, v135, v139
	v_max3_f32 v132, v132, v136, v140
	s_nop 1
	v_max_f32_dpp v132, v132, v132 quad_perm:[1,0,3,2] row_mask:0xf bank_mask:0xf
	s_nop 1
	v_max_f32_dpp v132, v132, v132 quad_perm:[2,3,0,1] row_mask:0xf bank_mask:0xf
	s_nop 1
	v_max_f32_dpp v132, v132, v132 row_half_mirror row_mask:0xf bank_mask:0xf
	s_nop 1
	v_max_f32_dpp v132, v132, v132 row_mirror row_mask:0xf bank_mask:0xf
	s_nop 1
	v_readlane_b32 s36, v132, 0
	v_readlane_b32 s37, v132, 16
	v_readlane_b32 s38, v132, 32
	v_readlane_b32 s39, v132, 48
	s_nop 2
	v_mov_b32_e32 v133, s36
	v_max_f32_e32 v133, s37, v133
	v_max_f32_e32 v133, s38, v133
	v_max_f32_e32 v133, s39, v133
	v_sqrt_f32_e32 v133, v133
	v_mov_b32_e32 v135, 0x3ca3d70a
	s_mov_b32 s36, 0xffff
	v_mul_f32_e32 v134, v141, v133
	v_mul_f32_e32 v136, v142, v133
	v_fmamk_f32 v134, v134, 0x3f804189, v135
	v_fmamk_f32 v136, v136, 0x3f804189, v135
	v_cvt_f16_f32_e64 v134, -v134
	v_cvt_f16_f32_e64 v136, -v136
	v_cmp_gt_u32_e32 vcc, 32, v1
	v_cvt_f32_f16_e32 v148, v134
	v_cvt_f32_f16_e32 v149, v136
	v_bfi_b32 v134, s36, v134, v11
	v_bfi_b32 v136, s36, v136, v15
	v_cndmask_b32_e32 v11, v11, v134, vcc
	v_cndmask_b32_e32 v15, v15, v136, vcc
	v_mov_b32_e32 v16, 0
	v_mov_b32_e32 v17, 0
	v_mov_b32_e32 v18, 0
	v_mov_b32_e32 v19, 0
	v_mov_b32_e32 v20, 0
	v_mov_b32_e32 v21, 0
	v_mov_b32_e32 v22, 0
	v_mov_b32_e32 v23, 0
	v_mov_b32_e32 v24, 0
	v_mov_b32_e32 v25, 0
	v_mov_b32_e32 v26, 0
	v_mov_b32_e32 v27, 0
	v_mov_b32_e32 v28, 0
	v_mov_b32_e32 v29, 0
	v_mov_b32_e32 v30, 0
	v_mov_b32_e32 v31, 0
	v_mov_b32_e32 v32, 0
	v_mov_b32_e32 v33, 0
	v_mov_b32_e32 v34, 0
	v_mov_b32_e32 v35, 0
	v_mov_b32_e32 v36, 0
	v_mov_b32_e32 v37, 0
	v_mov_b32_e32 v38, 0
	v_mov_b32_e32 v39, 0
	v_mov_b32_e32 v40, 0
	v_mov_b32_e32 v41, 0
	v_mov_b32_e32 v42, 0
	v_mov_b32_e32 v43, 0
	v_mov_b32_e32 v44, 0
	v_mov_b32_e32 v45, 0
	v_mov_b32_e32 v46, 0
	v_mov_b32_e32 v47, 0
	s_waitcnt vmcnt(0)
	s_barrier
	s_mov_b32 s28, 2
	s_sub_u32 s30, s28, s25
	s_mul_i32 s30, s30, 6
	s_add_u32 s30, s30, s24
	s_mul_i32 s31, s28, 6
	s_add_u32 s31, s31, s22
	s_cmp_lt_u32 s28, s25
	s_cselect_b32 s30, s31, s30
	s_lshl_b32 s33, s18, 10
	s_lshl_b32 s31, s30, 12
	s_add_u32 s31, s31, s33
	s_add_u32 s50, s8, s31
	s_addc_u32 s51, s9, 0
	s_add_u32 s52, s50, 0x3000
	s_addc_u32 s53, s51, 0
	s_add_u32 s34, s48, s33
	s_mov_b32 m0, s34
	s_add_u32 s35, s34, 0x3000
	global_load_lds_dwordx4 v2, s[50:51]
	s_mov_b32 m0, s35
	s_nop 0
	global_load_lds_dwordx4 v2, s[52:53]
	s_cmp_lt_u32 s18, 6
	s_cbranch_scc0 .Lm_nok_p2
	s_lshl_b32 s31, s30, 10
	s_add_u32 s31, s31, s33
	s_add_u32 s54, s4, s31
	s_addc_u32 s55, s5, 0
	s_add_u32 s34, s34, 24576
	s_mov_b32 m0, s34
	s_nop 0
	global_load_lds_dwordx4 v2, s[54:55]
.Lm_nok_p2:
	v_add_u32_e32 v128, s46, v2
	v_add_u32_e32 v129, s47, v2
	ds_read_b128 v[88:91], v128 offset:24576
	ds_read_b128 v[92:95], v128 offset:25600
	ds_read_b128 v[96:99], v128 offset:0
	ds_read_b128 v[104:107], v128 offset:2048
	ds_read_b128 v[100:103], v128 offset:1024
	ds_read_b128 v[108:111], v128 offset:3072
	s_waitcnt lgkmcnt(5)
	v_mfma_f32_32x32x16_f16 v[48:63], v[88:91], v[8:11], 0
	s_nop 5
.Lm_steps:
	s_waitcnt lgkmcnt(4)
	v_mfma_f32_32x32x16_f16 v[64:79], v[92:95], v[8:11], 0
	ds_read_b128 v[88:91], v128 offset:26624
	ds_read_b128 v[112:115], v128 offset:4096
	ds_read_b128 v[120:123], v128 offset:6144
	v_exp_f32_e32 v48, v48
	v_exp_f32_e32 v49, v49
	v_exp_f32_e32 v50, v50
	v_exp_f32_e32 v51, v51
	v_exp_f32_e32 v52, v52
	v_exp_f32_e32 v53, v53
	v_exp_f32_e32 v54, v54
	v_exp_f32_e32 v55, v55
	v_cvt_pk_bf16_f32 v80, v48, v49
	v_cvt_pk_bf16_f32 v81, v50, v51
	v_cvt_pk_bf16_f32 v82, v52, v53
	v_cvt_pk_bf16_f32 v83, v54, v55
	ds_read_b128 v[116:119], v128 offset:5120
	ds_read_b128 v[124:127], v128 offset:7168
	v_exp_f32_e32 v56, v56
	v_exp_f32_e32 v57, v57
	v_exp_f32_e32 v58, v58
	v_exp_f32_e32 v59, v59
	s_waitcnt lgkmcnt(7)
	v_mfma_f32_32x32x16_bf16 v[16:31], v[96:99], v[80:83], v[16:31]
	v_exp_f32_e32 v60, v60
	v_exp_f32_e32 v61, v61
	v_exp_f32_e32 v62, v62
	v_exp_f32_e32 v63, v63
	v_mfma_f32_32x32x16_bf16 v[32:47], v[104:107], v[80:83], v[32:47]
	v_cvt_pk_bf16_f32 v84, v56, v57
	v_cvt_pk_bf16_f32 v85, v58, v59
	v_cvt_pk_bf16_f32 v86, v60, v61
	v_cvt_pk_bf16_f32 v87, v62, v63
	s_waitcnt lgkmcnt(4)
	v_mfma_f32_32x32x16_f16 v[48:63], v[88:91], v[8:11], 0
	ds_read_b128 v[92:95], v128 offset:27648
	ds_read_b128 v[96:99], v128 offset:8192
	ds_read_b128 v[104:107], v128 offset:10240
	v_exp_f32_e32 v64, v64
	v_exp_f32_e32 v65, v65
	v_exp_f32_e32 v66, v66
	v_exp_f32_e32 v67, v67
	v_mfma_f32_32x32x16_bf16 v[16:31], v[100:103], v[84:87], v[16:31]
	v_exp_f32_e32 v68, v68
	v_exp_f32_e32 v69, v69
	v_exp_f32_e32 v70, v70
	v_exp_f32_e32 v71, v71
	v_mfma_f32_32x32x16_bf16 v[32:47], v[108:111], v[84:87], v[32:47]
	v_cvt_pk_bf16_f32 v80, v64, v65
	v_cvt_pk_bf16_f32 v81, v66, v67
	v_cvt_pk_bf16_f32 v82, v68, v69
	v_cvt_pk_bf16_f32 v83, v70, v71
	ds_read_b128 v[100:103], v128 offset:9216
	ds_read_b128 v[108:111], v128 offset:11264
	v_exp_f32_e32 v72, v72
	v_exp_f32_e32 v73, v73
	v_exp_f32_e32 v74, v74
	v_exp_f32_e32 v75, v75
	s_waitcnt lgkmcnt(7)
	v_mfma_f32_32x32x16_bf16 v[16:31], v[112:115], v[80:83], v[16:31]
	v_exp_f32_e32 v76, v76
	v_exp_f32_e32 v77, v77
	v_exp_f32_e32 v78, v78
	v_exp_f32_e32 v79, v79
	v_mfma_f32_32x32x16_bf16 v[32:47], v[120:123], v[80:83], v[32:47]
	v_cvt_pk_bf16_f32 v84, v72, v73
	v_cvt_pk_bf16_f32 v85, v74, v75
	v_cvt_pk_bf16_f32 v86, v76, v77
	v_cvt_pk_bf16_f32 v87, v78, v79
	s_waitcnt lgkmcnt(4)
	v_mfma_f32_32x32x16_f16 v[64:79], v[92:95], v[8:11], 0
	ds_read_b128 v[88:91], v128 offset:28672
	ds_read_b128 v[112:115], v128 offset:12288
	ds_read_b128 v[120:123], v128 offset:14336
	v_exp_f32_e32 v48, v48
	v_exp_f32_e32 v49, v49
	v_exp_f32_e32 v50, v50
	v_exp_f32_e32 v51, v51
	v_mfma_f32_32x32x16_bf16 v[16:31], v[116:119], v[84:87], v[16:31]
	v_exp_f32_e32 v52, v52
	v_exp_f32_e32 v53, v53
	v_exp_f32_e32 v54, v54
	v_exp_f32_e32 v55, v55
	v_mfma_f32_32x32x16_bf16 v[32:47], v[124:127], v[84:87], v[32:47]
	v_cvt_pk_bf16_f32 v80, v48, v49
	v_cvt_pk_bf16_f32 v81, v50, v51
	v_cvt_pk_bf16_f32 v82, v52, v53
	v_cvt_pk_bf16_f32 v83, v54, v55
	ds_read_b128 v[116:119], v128 offset:13312
	ds_read_b128 v[124:127], v128 offset:15360
	v_exp_f32_e32 v56, v56
	v_exp_f32_e32 v57, v57
	v_exp_f32_e32 v58, v58
	v_exp_f32_e32 v59, v59
	s_waitcnt lgkmcnt(7)
	v_mfma_f32_32x32x16_bf16 v[16:31], v[96:99], v[80:83], v[16:31]
	v_exp_f32_e32 v60, v60
	v_exp_f32_e32 v61, v61
	v_exp_f32_e32 v62, v62
	v_exp_f32_e32 v63, v63
	v_mfma_f32_32x32x16_bf16 v[32:47], v[104:107], v[80:83], v[32:47]
	v_cvt_pk_bf16_f32 v84, v56, v57
	v_cvt_pk_bf16_f32 v85, v58, v59
	v_cvt_pk_bf16_f32 v86, v60, v61
	v_cvt_pk_bf16_f32 v87, v62, v63
	s_waitcnt lgkmcnt(4)
	v_mfma_f32_32x32x16_f16 v[48:63], v[88:91], v[8:11], 0
	ds_read_b128 v[92:95], v128 offset:29696
	ds_read_b128 v[96:99], v128 offset:16384
	ds_read_b128 v[104:107], v128 offset:18432
	v_exp_f32_e32 v64, v64
	v_exp_f32_e32 v65, v65
	v_exp_f32_e32 v66, v66
	v_exp_f32_e32 v67, v67
	v_mfma_f32_32x32x16_bf16 v[16:31], v[100:103], v[84:87], v[16:31]
	v_exp_f32_e32 v68, v68
	v_exp_f32_e32 v69, v69
	v_exp_f32_e32 v70, v70
	v_exp_f32_e32 v71, v71
	v_mfma_f32_32x32x16_bf16 v[32:47], v[108:111], v[84:87], v[32:47]
	v_cvt_pk_bf16_f32 v80, v64, v65
	v_cvt_pk_bf16_f32 v81, v66, v67
	v_cvt_pk_bf16_f32 v82, v68, v69
	v_cvt_pk_bf16_f32 v83, v70, v71
	ds_read_b128 v[100:103], v128 offset:17408
	ds_read_b128 v[108:111], v128 offset:19456
	v_exp_f32_e32 v72, v72
	v_exp_f32_e32 v73, v73
	v_exp_f32_e32 v74, v74
	v_exp_f32_e32 v75, v75
	s_waitcnt lgkmcnt(7)
	v_mfma_f32_32x32x16_bf16 v[16:31], v[112:115], v[80:83], v[16:31]
	v_exp_f32_e32 v76, v76
	v_exp_f32_e32 v77, v77
	v_exp_f32_e32 v78, v78
	v_exp_f32_e32 v79, v79
	v_mfma_f32_32x32x16_bf16 v[32:47], v[120:123], v[80:83], v[32:47]
	v_cvt_pk_bf16_f32 v84, v72, v73
	v_cvt_pk_bf16_f32 v85, v74, v75
	v_cvt_pk_bf16_f32 v86, v76, v77
	v_cvt_pk_bf16_f32 v87, v78, v79
	s_waitcnt lgkmcnt(4)
	v_mfma_f32_32x32x16_f16 v[64:79], v[92:95], v[8:11], 0
	ds_read_b128 v[88:91], v129 offset:24576
	ds_read_b128 v[112:115], v128 offset:20480
	ds_read_b128 v[120:123], v128 offset:22528
	v_exp_f32_e32 v48, v48
	v_exp_f32_e32 v49, v49
	v_exp_f32_e32 v50, v50
	v_exp_f32_e32 v51, v51
	v_mfma_f32_32x32x16_bf16 v[16:31], v[116:119], v[84:87], v[16:31]
	v_exp_f32_e32 v52, v52
	v_exp_f32_e32 v53, v53
	v_exp_f32_e32 v54, v54
	v_exp_f32_e32 v55, v55
	v_mfma_f32_32x32x16_bf16 v[32:47], v[124:127], v[84:87], v[32:47]
	v_cvt_pk_bf16_f32 v80, v48, v49
	v_cvt_pk_bf16_f32 v81, v50, v51
	v_cvt_pk_bf16_f32 v82, v52, v53
	v_cvt_pk_bf16_f32 v83, v54, v55
	ds_read_b128 v[116:119], v128 offset:21504
	ds_read_b128 v[124:127], v128 offset:23552
	v_exp_f32_e32 v56, v56
	v_exp_f32_e32 v57, v57
	v_exp_f32_e32 v58, v58
	v_exp_f32_e32 v59, v59
	s_waitcnt lgkmcnt(7)
	v_mfma_f32_32x32x16_bf16 v[16:31], v[96:99], v[80:83], v[16:31]
	v_exp_f32_e32 v60, v60
	v_exp_f32_e32 v61, v61
	v_exp_f32_e32 v62, v62
	v_exp_f32_e32 v63, v63
	v_mfma_f32_32x32x16_bf16 v[32:47], v[104:107], v[80:83], v[32:47]
	v_cvt_pk_bf16_f32 v84, v56, v57
	v_cvt_pk_bf16_f32 v85, v58, v59
	v_cvt_pk_bf16_f32 v86, v60, v61
	v_cvt_pk_bf16_f32 v87, v62, v63
	s_waitcnt lgkmcnt(4)
	v_mfma_f32_32x32x16_f16 v[48:63], v[88:91], v[8:11], 0
	ds_read_b128 v[92:95], v129 offset:25600
	ds_read_b128 v[96:99], v129 offset:0
	ds_read_b128 v[104:107], v129 offset:2048
	v_exp_f32_e32 v64, v64
	v_exp_f32_e32 v65, v65
	v_exp_f32_e32 v66, v66
	v_exp_f32_e32 v67, v67
	v_mfma_f32_32x32x16_bf16 v[16:31], v[100:103], v[84:87], v[16:31]
	v_exp_f32_e32 v68, v68
	v_exp_f32_e32 v69, v69
	v_exp_f32_e32 v70, v70
	v_exp_f32_e32 v71, v71
	v_mfma_f32_32x32x16_bf16 v[32:47], v[108:111], v[84:87], v[32:47]
	v_cvt_pk_bf16_f32 v80, v64, v65
	v_cvt_pk_bf16_f32 v81, v66, v67
	v_cvt_pk_bf16_f32 v82, v68, v69
	v_cvt_pk_bf16_f32 v83, v70, v71
	ds_read_b128 v[100:103], v129 offset:1024
	ds_read_b128 v[108:111], v129 offset:3072
	v_exp_f32_e32 v72, v72
	v_exp_f32_e32 v73, v73
	v_exp_f32_e32 v74, v74
	v_exp_f32_e32 v75, v75
	s_waitcnt lgkmcnt(7)
	v_mfma_f32_32x32x16_bf16 v[16:31], v[112:115], v[80:83], v[16:31]
	v_exp_f32_e32 v76, v76
	v_exp_f32_e32 v77, v77
	v_exp_f32_e32 v78, v78
	v_exp_f32_e32 v79, v79
	v_mfma_f32_32x32x16_bf16 v[32:47], v[120:123], v[80:83], v[32:47]
	v_cvt_pk_bf16_f32 v84, v72, v73
	v_cvt_pk_bf16_f32 v85, v74, v75
	v_cvt_pk_bf16_f32 v86, v76, v77
	v_cvt_pk_bf16_f32 v87, v78, v79
	s_waitcnt lgkmcnt(5)
	s_nop 0
	v_mfma_f32_32x32x16_bf16 v[16:31], v[116:119], v[84:87], v[16:31]
	v_mfma_f32_32x32x16_bf16 v[32:47], v[124:127], v[84:87], v[32:47]
	s_mov_b32 s30, s46
	s_mov_b32 s46, s47
	s_mov_b32 s47, s48
	s_mov_b32 s48, s30
	s_add_u32 s27, s27, 1
	s_cmp_lt_u32 s27, 9
	s_cbranch_scc0 .Lm_flush
	s_cmp_eq_u32 s27, s25
	s_cbranch_scc1 .Lm_flush
	s_waitcnt vmcnt(0)
.Lm_bar:
	s_barrier
	v_add_u32_e32 v128, s46, v2
	v_add_u32_e32 v129, s47, v2
	s_add_u32 s28, s27, 2
	s_cmp_lt_u32 s28, 9
	s_cbranch_scc0 .Lm_steps
	s_sub_u32 s30, s28, s25
	s_mul_i32 s30, s30, 6
	s_add_u32 s30, s30, s24
	s_mul_i32 s31, s28, 6
	s_add_u32 s31, s31, s22
	s_cmp_lt_u32 s28, s25
	s_cselect_b32 s30, s31, s30
	s_lshl_b32 s33, s18, 10
	s_lshl_b32 s31, s30, 12
	s_add_u32 s31, s31, s33
	s_add_u32 s50, s8, s31
	s_addc_u32 s51, s9, 0
	s_add_u32 s52, s50, 0x3000
	s_addc_u32 s53, s51, 0
	s_add_u32 s34, s48, s33
	s_mov_b32 m0, s34
	s_add_u32 s35, s34, 0x3000
	global_load_lds_dwordx4 v2, s[50:51]
	s_mov_b32 m0, s35
	s_nop 0
	global_load_lds_dwordx4 v2, s[52:53]
	s_cmp_lt_u32 s18, 6
	s_cbranch_scc0 .Lm_nok_lp
	s_lshl_b32 s31, s30, 10
	s_add_u32 s31, s31, s33
	s_add_u32 s54, s4, s31
	s_addc_u32 s55, s5, 0
	s_add_u32 s34, s34, 24576
	s_mov_b32 m0, s34
	s_nop 0
	global_load_lds_dwordx4 v2, s[54:55]
.Lm_nok_lp:
	s_branch .Lm_steps
.Lm_flush:
	s_nop 15
	v_rcp_f32_e32 v130, v42
	v_cmp_lt_f32_e32 vcc, 0, v42
	s_mul_i32 s40, s29, 0x180
	s_lshl_b32 s41, s18, 5
	v_fma_f32 v131, -v42, v130, 1.0
	s_add_u32 s40, s40, s41
	s_lshl_b32 s44, s40, 2
	v_fma_f32 v130, v131, v130, v130
	s_mul_i32 s45, s40, 0x68
	s_add_u32 s42, s16, s44
	s_addc_u32 s43, s17, 0
	v_cndmask_b32_e32 v130, 0, v130, vcc
	s_add_u32 s40, s14, s45
	s_addc_u32 s41, s15, 0
	v_mul_f32_e32 v132, v16, v130
	v_mul_f32_e32 v133, v17, v130
	v_mul_f32_e32 v134, v18, v130
	v_mul_f32_e32 v135, v19, v130
	v_cvt_pk_f16_f32 v136, v132, v133
	v_cvt_pk_f16_f32 v137, v134, v135
	ds_write_b64 v6, v[136:137] offset:0
	v_mul_f32_e32 v132, v20, v130
	v_mul_f32_e32 v133, v21, v130
	v_mul_f32_e32 v134, v22, v130
	v_mul_f32_e32 v135, v23, v130
	v_cvt_pk_f16_f32 v136, v132, v133
	v_cvt_pk_f16_f32 v137, v134, v135
	ds_write_b64 v6, v[136:137] offset:16
	v_mul_f32_e32 v132, v24, v130
	v_mul_f32_e32 v133, v25, v130
	v_mul_f32_e32 v134, v26, v130
	v_mul_f32_e32 v135, v27, v130
	v_cvt_pk_f16_f32 v136, v132, v133
	v_cvt_pk_f16_f32 v137, v134, v135
	ds_write_b64 v6, v[136:137] offset:32
	v_mul_f32_e32 v132, v28, v130
	v_mul_f32_e32 v133, v29, v130
	v_mul_f32_e32 v134, v30, v130
	v_mul_f32_e32 v135, v31, v130
	v_cvt_pk_f16_f32 v136, v132, v133
	v_cvt_pk_f16_f32 v137, v134, v135
	ds_write_b64 v6, v[136:137] offset:48
	v_mul_f32_e32 v132, v32, v130
	v_mul_f32_e32 v133, v33, v130
	v_mul_f32_e32 v134, v34, v130
	v_mul_f32_e32 v135, v35, v130
	v_cvt_pk_f16_f32 v136, v132, v133
	v_cvt_pk_f16_f32 v137, v134, v135
	ds_write_b64 v6, v[136:137] offset:64
	v_mul_f32_e32 v132, v36, v130
	v_mul_f32_e32 v133, v37, v130
	v_mul_f32_e32 v134, v38, v130
	v_mul_f32_e32 v135, v39, v130
	v_cvt_pk_f16_f32 v136, v132, v133
	v_cvt_pk_f16_f32 v137, v134, v135
	ds_write_b64 v6, v[136:137] offset:80
	s_mov_b32 exec_hi, 0
	v_mul_f32_e32 v132, v40, v130
	v_mul_f32_e32 v133, v41, v130
	v_mul_f32_e32 v134, v42, v130
	v_mul_f32_e32 v135, v43, v130
	v_cvt_pk_f16_f32 v136, v132, v133
	v_cvt_pk_f16_f32 v137, v134, v135
	ds_write_b64 v6, v[136:137] offset:96
	s_mov_b64 exec, -1
	s_waitcnt lgkmcnt(0)
	ds_read_b128 v[132:135], v7 offset:0
	ds_read_b128 v[136:139], v7 offset:1024
	ds_read_b128 v[140:143], v7 offset:2048
	ds_read_b128 v[144:147], v7 offset:3072
	v_log_f32_e32 v131, v42
	s_waitcnt lgkmcnt(0)
	v_sub_f32_e32 v131, v131, v148
	global_store_dwordx4 v2, v[132:135], s[40:41] offset:0 nt
	global_store_dwordx4 v2, v[136:139], s[40:41] offset:1024 nt
	global_store_dwordx4 v2, v[140:143], s[40:41] offset:2048 nt
	v_cndmask_b32_e32 v131, v150, v131, vcc
	s_mov_b32 exec_lo, 0xffff
	s_mov_b32 exec_hi, 0
	global_store_dwordx4 v2, v[144:147], s[40:41] offset:3072 nt
	s_mov_b32 exec_lo, -1
	global_store_dword v5, v131, s[42:43]
	s_mov_b64 exec, -1
	s_cmp_lt_u32 s27, 9
	s_cbranch_scc1 .Lm_switch
	s_endpgm
.Lm_switch:
	v_mov_b32_e32 v8, v12
	v_mov_b32_e32 v9, v13
	v_mov_b32_e32 v10, v14
	v_mov_b32_e32 v11, v15
	v_mov_b32_e32 v148, v149
	s_add_u32 s29, s23, 0x100
	v_mov_b32_e32 v16, 0
	v_mov_b32_e32 v17, 0
	v_mov_b32_e32 v18, 0
	v_mov_b32_e32 v19, 0
	v_mov_b32_e32 v20, 0
	v_mov_b32_e32 v21, 0
	v_mov_b32_e32 v22, 0
	v_mov_b32_e32 v23, 0
	v_mov_b32_e32 v24, 0
	v_mov_b32_e32 v25, 0
	v_mov_b32_e32 v26, 0
	v_mov_b32_e32 v27, 0
	v_mov_b32_e32 v28, 0
	v_mov_b32_e32 v29, 0
	v_mov_b32_e32 v30, 0
	v_mov_b32_e32 v31, 0
	v_mov_b32_e32 v32, 0
	v_mov_b32_e32 v33, 0
	v_mov_b32_e32 v34, 0
	v_mov_b32_e32 v35, 0
	v_mov_b32_e32 v36, 0
	v_mov_b32_e32 v37, 0
	v_mov_b32_e32 v38, 0
	v_mov_b32_e32 v39, 0
	v_mov_b32_e32 v40, 0
	v_mov_b32_e32 v41, 0
	v_mov_b32_e32 v42, 0
	v_mov_b32_e32 v43, 0
	v_mov_b32_e32 v44, 0
	v_mov_b32_e32 v45, 0
	v_mov_b32_e32 v46, 0
	v_mov_b32_e32 v47, 0
	v_mfma_f32_32x32x16_f16 v[48:63], v[88:91], v[8:11], 0
	s_waitcnt vmcnt(5)
	s_branch .Lm_bar

	.amdhsa_kernel _Z8pam_mainPKDv4_jS1_S1_PKfS3_PDF16_Pf
		.amdhsa_group_segment_fixed_size 133120
		.amdhsa_private_segment_fixed_size 0
		.amdhsa_kernarg_size 56
		.amdhsa_user_sgpr_count 2
		.amdhsa_user_sgpr_dispatch_ptr 0
		.amdhsa_user_sgpr_queue_ptr 0
		.amdhsa_user_sgpr_kernarg_segment_ptr 1
		.amdhsa_user_sgpr_dispatch_id 0
		.amdhsa_user_sgpr_kernarg_preload_length 0
		.amdhsa_user_sgpr_kernarg_preload_offset 0
		.amdhsa_user_sgpr_private_segment_size 0
		.amdhsa_uses_dynamic_stack 0
		.amdhsa_enable_private_segment 0
		.amdhsa_system_sgpr_workgroup_id_x 1
		.amdhsa_system_sgpr_workgroup_id_y 0
		.amdhsa_system_sgpr_workgroup_id_z 0
		.amdhsa_system_sgpr_workgroup_info 0
		.amdhsa_system_vgpr_workitem_id 0
		.amdhsa_next_free_vgpr 152
		.amdhsa_next_free_sgpr 96
		.amdhsa_accum_offset 152
		.amdhsa_reserve_vcc 1
		.amdhsa_float_round_mode_32 0
		.amdhsa_float_round_mode_16_64 0
		.amdhsa_float_denorm_mode_32 3
		.amdhsa_float_denorm_mode_16_64 3
		.amdhsa_dx10_clamp 1
		.amdhsa_ieee_mode 1
		.amdhsa_fp16_overflow 0
		.amdhsa_tg_split 0
		.amdhsa_exception_fp_ieee_invalid_op 0
		.amdhsa_exception_fp_denorm_src 0
		.amdhsa_exception_fp_ieee_div_zero 0
		.amdhsa_exception_fp_ieee_overflow 0
		.amdhsa_exception_fp_ieee_underflow 0
		.amdhsa_exception_fp_ieee_inexact 0
		.amdhsa_exception_int_div_zero 0
	.end_amdhsa_kernel

amdhsa.kernels:
  - .agpr_count:     16
    .args:
      - .actual_access:  read_only
        .address_space:  global
        .offset:         0
        .size:           8
        .value_kind:     global_buffer
      - .actual_access:  read_only
        .address_space:  global
        .offset:         8
        .size:           8
        .value_kind:     global_buffer
      - .actual_access:  read_only
        .address_space:  global
        .offset:         16
        .size:           8
        .value_kind:     global_buffer
      - .actual_access:  read_only
        .address_space:  global
        .offset:         24
        .size:           8
        .value_kind:     global_buffer
      - .actual_access:  write_only
        .address_space:  global
        .offset:         32
        .size:           8
        .value_kind:     global_buffer
      - .actual_access:  write_only
        .address_space:  global
        .offset:         40
        .size:           8
        .value_kind:     global_buffer
      - .actual_access:  write_only
        .address_space:  global
        .offset:         48
        .size:           8
        .value_kind:     global_buffer
      - .actual_access:  write_only
        .address_space:  global
        .offset:         56
        .size:           8
        .value_kind:     global_buffer
      - .actual_access:  write_only
        .address_space:  global
        .offset:         64
        .size:           8
        .value_kind:     global_buffer
    .group_segment_fixed_size: 29184
    .kernarg_segment_align: 8
    .kernarg_segment_size: 72
    .language:       OpenCL C
    .language_version:
      - 2
      - 0
    .max_flat_workgroup_size: 256
    .name:           _Z8pam_prepPKfS0_S0_S0_PDv4_jS2_S2_PfS3_
    .private_segment_fixed_size: 0
    .sgpr_count:     28
    .sgpr_spill_count: 0
    .symbol:         _Z8pam_prepPKfS0_S0_S0_PDv4_jS2_S2_PfS3_.kd
    .uniform_work_group_size: 1
    .uses_dynamic_stack: false
    .vgpr_count:     52
    .vgpr_spill_count: 0
    .wavefront_size: 64
  - .agpr_count:     0
    .args:
      - .address_space:  global
        .offset:         0
        .size:           8
        .value_kind:     global_buffer
      - .actual_access:  read_only
        .address_space:  global
        .offset:         8
        .size:           8
        .value_kind:     global_buffer
      - .address_space:  global
        .offset:         16
        .size:           8
        .value_kind:     global_buffer
      - .actual_access:  read_only
        .address_space:  global
        .offset:         24
        .size:           8
        .value_kind:     global_buffer
      - .actual_access:  read_only
        .address_space:  global
        .offset:         32
        .size:           8
        .value_kind:     global_buffer
      - .actual_access:  write_only
        .address_space:  global
        .offset:         40
        .size:           8
        .value_kind:     global_buffer
      - .actual_access:  write_only
        .address_space:  global
        .offset:         48
        .size:           8
        .value_kind:     global_buffer
    .group_segment_fixed_size: 133120
    .kernarg_segment_align: 8
    .kernarg_segment_size: 56
    .language:       OpenCL C
    .language_version:
      - 2
      - 0
    .max_flat_workgroup_size: 768
    .name:           _Z8pam_mainPKDv4_jS1_S1_PKfS3_PDF16_Pf
    .private_segment_fixed_size: 0
    .sgpr_count:     52
    .sgpr_spill_count: 0
    .symbol:         _Z8pam_mainPKDv4_jS1_S1_PKfS3_PDF16_Pf.kd
    .uniform_work_group_size: 1
    .uses_dynamic_stack: false
    .vgpr_count:     152
    .vgpr_spill_count: 0
    .wavefront_size: 64
  - .agpr_count:     0
    .args:
      - .actual_access:  read_only
        .address_space:  global
        .offset:         0
        .size:           8
        .value_kind:     global_buffer
      - .actual_access:  read_only
        .address_space:  global
        .offset:         8
        .size:           8
        .value_kind:     global_buffer
      - .actual_access:  read_only
        .address_space:  global
        .offset:         16
        .size:           8
        .value_kind:     global_buffer
      - .actual_access:  read_only
        .address_space:  global
        .offset:         24
        .size:           8
        .value_kind:     global_buffer
      - .actual_access:  write_only
        .address_space:  global
        .offset:         32
        .size:           8
        .value_kind:     global_buffer
    .group_segment_fixed_size: 0
    .kernarg_segment_align: 8
    .kernarg_segment_size: 40
    .language:       OpenCL C
    .language_version:
      - 2
      - 0
    .max_flat_workgroup_size: 256
    .name:           _Z11pam_combinePKDF16_PKfS2_S2_Pf
    .private_segment_fixed_size: 0
    .sgpr_count:     23
    .sgpr_spill_count: 0
    .symbol:         _Z11pam_combinePKDF16_PKfS2_S2_Pf.kd
    .uniform_work_group_size: 1
    .uses_dynamic_stack: false
    .vgpr_count:     68
    .vgpr_spill_count: 0
    .wavefront_size: 64
